# P6 epilogue: gate row and next-layer shift row staged once per 4-token pass in spare LDS (0x10000..0x12000), X1 touch loads retargeted to the placeholder register
# speedup vs baseline: 1.0094x; 1.0047x over previous
.LBB0_975:
	s_add_i32 s0, s96, s35
	s_ashr_i32 s1, s0, 31
	s_lshr_b32 s1, s1, 19
	s_add_i32 s0, s0, s1
	s_ashr_i32 s2, s0, 13
	s_xor_b64 s[14:15], s[6:7], -1
	s_ashr_i32 s0, s2, 31
	s_add_u32 s1, s2, s87
	s_addc_u32 s0, s0, 0
	s_waitcnt vmcnt(0)
	v_lshlrev_b32_e32 v186, 6, v179
	v_lshl_add_u32 v185, v179, 4, s85
	v_mov_b32_e32 v187, 0
	global_load_dwordx4 v[8:11], v186, s[16:17] offset:0
	global_load_dwordx4 v[12:15], v186, s[16:17] offset:16
	global_load_dwordx4 v[16:19], v186, s[16:17] offset:32
	global_load_dwordx4 v[20:23], v186, s[16:17] offset:48
	global_load_dwordx4 v[24:27], v186, s[28:29] offset:0
	global_load_dwordx4 v[28:31], v186, s[28:29] offset:16
	global_load_dwordx4 v[32:35], v186, s[28:29] offset:32
	global_load_dwordx4 v[36:39], v186, s[28:29] offset:48
	global_load_dwordx4 v[40:43], v186, s[12:13] offset:0
	global_load_dwordx4 v[44:47], v186, s[12:13] offset:16
	global_load_dwordx4 v[48:51], v186, s[12:13] offset:32
	global_load_dwordx4 v[52:55], v186, s[12:13] offset:48
	global_load_dwordx4 v[56:59], v186, s[90:91] offset:0
	global_load_dwordx4 v[60:63], v186, s[90:91] offset:16
	global_load_dwordx4 v[64:67], v186, s[90:91] offset:32
	global_load_dwordx4 v[68:71], v186, s[90:91] offset:48
	s_waitcnt vmcnt(0)
	ds_write_b128 v185, v[8:11] offset:0
	ds_write_b128 v185, v[12:15] offset:1024
	ds_write_b128 v185, v[16:19] offset:2048
	ds_write_b128 v185, v[20:23] offset:3072
	ds_write_b128 v185, v[24:27] offset:4096
	ds_write_b128 v185, v[28:31] offset:5120
	ds_write_b128 v185, v[32:35] offset:6144
	ds_write_b128 v185, v[36:39] offset:7168
	ds_write_b128 v185, v[40:43] offset:8192
	ds_write_b128 v185, v[44:47] offset:9216
	ds_write_b128 v185, v[48:51] offset:10240
	ds_write_b128 v185, v[52:55] offset:11264
	ds_write_b128 v185, v[56:59] offset:12288
	ds_write_b128 v185, v[60:63] offset:13312
	ds_write_b128 v185, v[64:67] offset:14336
	ds_write_b128 v185, v[68:71] offset:15360
	s_waitcnt lgkmcnt(0)
	s_mul_i32 s40, s1, 0x6000
	s_add_u32 s40, s70, s40
	s_addc_u32 s41, s71, 0
	s_add_u32 s42, s40, 0x5000
	s_addc_u32 s43, s41, 0
	s_add_u32 s40, s40, 0x18000
	s_addc_u32 s41, s41, 0
	v_mov_b32_e32 v188, 0x10000
	v_lshl_add_u32 v188, v179, 4, v188
	global_load_dwordx4 v[8:11], v186, s[42:43] offset:0
	global_load_dwordx4 v[12:15], v186, s[42:43] offset:16
	global_load_dwordx4 v[16:19], v186, s[42:43] offset:32
	global_load_dwordx4 v[20:23], v186, s[42:43] offset:48
	global_load_dwordx4 v[24:27], v186, s[40:41] offset:0
	global_load_dwordx4 v[28:31], v186, s[40:41] offset:16
	global_load_dwordx4 v[32:35], v186, s[40:41] offset:32
	global_load_dwordx4 v[36:39], v186, s[40:41] offset:48
	s_waitcnt vmcnt(0)
	ds_write_b128 v188, v[8:11] offset:0
	ds_write_b128 v188, v[12:15] offset:1024
	ds_write_b128 v188, v[16:19] offset:2048
	ds_write_b128 v188, v[20:23] offset:3072
	ds_write_b128 v188, v[24:27] offset:4096
	ds_write_b128 v188, v[28:31] offset:5120
	ds_write_b128 v188, v[32:35] offset:6144
	ds_write_b128 v188, v[36:39] offset:7168
	s_waitcnt lgkmcnt(0)
	v_readlane_b32 s40, v253, 62
	v_readlane_b32 s41, v253, 63
	s_lshl_b64 s[44:45], s[96:97], 12
	v_lshlrev_b32_e32 v2, 6, v179
	s_add_u32 s40, s40, s44
	s_addc_u32 s41, s41, s45
	s_add_u32 s40, s40, 0x1000
	s_addc_u32 s41, s41, 0
	global_load_dword v184, v2, s[40:41]
	s_add_u32 s40, s40, 0x1000
	s_addc_u32 s41, s41, 0
	global_load_dword v184, v2, s[40:41]
	s_add_u32 s40, s40, 0x1000
	s_addc_u32 s41, s41, 0
	global_load_dword v184, v2, s[40:41]
	v_mov_b32_e32 v1, v179
	s_mulk_i32 s0, 0x6000
	s_mul_hi_u32 s3, s1, 0x6000
	s_add_i32 s3, s3, s0
	s_mulk_i32 s1, 0x6000
	v_lshlrev_b32_e32 v20, 4, v1
	s_add_u32 s6, s70, s1
	v_readlane_b32 s36, v253, 60
	v_ashrrev_i32_e32 v21, 31, v20
	s_addc_u32 s7, s71, s3
	s_lshl_b64 s[0:1], s[96:97], 12
	v_readlane_b32 s38, v253, 62
	v_lshlrev_b64 v[22:23], 2, v[20:21]
	v_readlane_b32 s39, v253, 63
	s_add_u32 s20, s38, s0
	v_lshl_add_u64 v[68:69], s[6:7], 0, v[22:23]
	s_mov_b64 s[6:7], 0x5000
	s_addc_u32 s21, s39, s1
	v_lshl_add_u64 v[12:13], v[68:69], 0, s[6:7]
	s_lshl_b64 s[6:7], s[96:97], 3
	v_lshl_add_u64 v[32:33], s[20:21], 0, v[22:23]
	s_add_u32 s6, s64, s6
	ds_read_b128 v[4:7], v188 offset:3072
	global_load_dword v184, v187, s[70:71]
	ds_read_b128 v[8:11], v188 offset:2048
	global_load_dword v184, v187, s[70:71]
	s_addc_u32 s7, s65, s7
	ds_read_b128 v[12:15], v188 offset:1024
	global_load_dword v184, v187, s[70:71]
	s_nop 0
	global_load_dwordx2 v[72:73], v3, s[6:7]
	global_load_dwordx4 v[16:19], v[32:33], off
	global_load_dwordx4 v[24:27], v[32:33], off offset:16
	global_load_dwordx4 v[28:31], v[32:33], off offset:32
	s_nop 0
	global_load_dwordx4 v[32:35], v[32:33], off offset:48
	v_lshl_add_u64 v[60:61], s[16:17], 0, v[22:23]
	v_lshl_add_u64 v[64:65], s[28:29], 0, v[22:23]
	v_add_co_u32_e32 v68, vcc, s18, v68
	ds_read_b128 v[36:39], v185 offset:7168
	global_load_dword v184, v187, s[28:29]
	ds_read_b128 v[40:43], v185 offset:3072
	global_load_dword v184, v187, s[16:17]
	ds_read_b128 v[44:47], v185 offset:2048
	global_load_dword v184, v187, s[16:17]
	ds_read_b128 v[48:51], v185 offset:6144
	global_load_dword v184, v187, s[28:29]
	ds_read_b128 v[52:55], v185 offset:5120
	global_load_dword v184, v187, s[28:29]
	ds_read_b128 v[56:59], v185 offset:1024
	global_load_dword v184, v187, s[16:17]
	s_nop 0
	ds_read_b128 v[60:63], v185 offset:0
	global_load_dword v184, v187, s[16:17]
	s_nop 0
	ds_read_b128 v[64:67], v185 offset:4096
	global_load_dword v184, v187, s[28:29]
	v_addc_co_u32_e32 v69, vcc, 0, v69, vcc
	ds_read_b128 v[68:71], v188 offset:0
	global_load_dword v184, v187, s[70:71]
	v_add_u32_e32 v142, 64, v183
	v_xor_b32_e32 v1, 1, v178
	v_xor_b32_e32 v2, 2, v178
	v_cmp_lt_i32_e32 vcc, v1, v142
	v_xor_b32_e32 v74, 4, v178
	v_readlane_b32 s20, v255, 42
	v_cndmask_b32_e32 v1, v178, v1, vcc
	v_cmp_lt_i32_e32 vcc, v2, v142
	v_readlane_b32 s22, v255, 44
	s_add_u32 s0, s30, s0
	v_cndmask_b32_e32 v75, v178, v2, vcc
	v_lshlrev_b32_e32 v2, 2, v1
	v_lshlrev_b32_e32 v1, 2, v75
	v_cmp_lt_i32_e32 vcc, v74, v142
	s_addc_u32 s1, s31, s1
	v_readlane_b32 s37, v253, 61
	v_readlane_b32 s40, v254, 0
	v_readlane_b32 s41, v254, 1
	v_readlane_b32 s42, v254, 2
	v_readlane_b32 s43, v254, 3
	v_readlane_b32 s44, v254, 4
	v_readlane_b32 s45, v254, 5
	v_readlane_b32 s46, v254, 6
	v_readlane_b32 s47, v254, 7
	v_readlane_b32 s48, v254, 8
	v_readlane_b32 s49, v254, 9
	v_readlane_b32 s50, v254, 10
	v_readlane_b32 s51, v254, 11
	v_readlane_b32 s21, v255, 43
	v_readlane_b32 s23, v255, 45
	s_waitcnt lgkmcnt(0)
	s_waitcnt vmcnt(14)
	v_pk_add_f32 v[12:13], v[12:13], 1.0 op_sel_hi:[1,0]
	v_pk_add_f32 v[14:15], v[14:15], 1.0 op_sel_hi:[1,0]
	s_waitcnt lgkmcnt(0)
	s_waitcnt vmcnt(12)
	v_pk_add_f32 v[18:19], v[18:19], v[72:73] op_sel_hi:[1,0] neg_lo:[0,1] neg_hi:[0,1]
	v_pk_add_f32 v[4:5], v[4:5], 1.0 op_sel_hi:[1,0]
	v_pk_mul_f32 v[18:19], v[72:73], v[18:19] op_sel:[1,0]
	s_waitcnt lgkmcnt(0)
	s_waitcnt vmcnt(9)
	v_pk_add_f32 v[32:33], v[32:33], v[72:73] op_sel_hi:[1,0] neg_lo:[0,1] neg_hi:[0,1]
	v_pk_add_f32 v[34:35], v[34:35], v[72:73] op_sel_hi:[1,0] neg_lo:[0,1] neg_hi:[0,1]
	v_pk_mul_f32 v[32:33], v[72:73], v[32:33] op_sel:[1,0]
	v_pk_mul_f32 v[34:35], v[72:73], v[34:35] op_sel:[1,0]
	s_waitcnt lgkmcnt(0)
	s_waitcnt vmcnt(7)
	v_pk_fma_f32 v[32:33], v[32:33], v[40:41], v[36:37]
	v_pk_fma_f32 v[34:35], v[34:35], v[42:43], v[38:39]
	v_pk_mul_f32 v[32:33], v[32:33], s[34:35] op_sel_hi:[1,0]
	v_pk_add_f32 v[6:7], v[6:7], 1.0 op_sel_hi:[1,0]
	v_pk_add_f32 v[24:25], v[24:25], v[72:73] op_sel_hi:[1,0] neg_lo:[0,1] neg_hi:[0,1]
	v_pk_mul_f32 v[34:35], v[34:35], s[34:35] op_sel_hi:[1,0]
	v_pk_fma_f32 v[42:43], v[138:139], v[4:5], v[32:33]
	s_waitcnt lgkmcnt(0)
	s_waitcnt vmcnt(1)
	v_pk_fma_f32 v[4:5], v[18:19], v[62:63], v[66:67]
	v_pk_add_f32 v[16:17], v[16:17], v[72:73] op_sel_hi:[1,0] neg_lo:[0,1] neg_hi:[0,1]
	v_pk_mul_f32 v[24:25], v[72:73], v[24:25] op_sel:[1,0]
	v_pk_fma_f32 v[40:41], v[140:141], v[6:7], v[34:35]
	v_pk_mul_f32 v[4:5], v[4:5], s[34:35] op_sel_hi:[1,0]
	s_waitcnt lgkmcnt(0)
	s_waitcnt vmcnt(0)
	v_pk_add_f32 v[6:7], v[70:71], 1.0 op_sel_hi:[1,0]
	v_pk_fma_f32 v[24:25], v[24:25], v[56:57], v[52:53]
	v_pk_fma_f32 v[52:53], v[128:129], v[6:7], v[4:5]
	v_pk_mul_f32 v[4:5], v[72:73], v[16:17] op_sel:[1,0]
	v_pk_add_f32 v[26:27], v[26:27], v[72:73] op_sel_hi:[1,0] neg_lo:[0,1] neg_hi:[0,1]
	v_pk_fma_f32 v[4:5], v[60:61], v[4:5], v[64:65]
	v_pk_mul_f32 v[26:27], v[72:73], v[26:27] op_sel:[1,0]
	v_pk_mul_f32 v[4:5], v[4:5], s[34:35] op_sel_hi:[1,0]
	v_pk_add_f32 v[6:7], v[68:69], 1.0 op_sel_hi:[1,0]
	v_pk_fma_f32 v[26:27], v[26:27], v[58:59], v[54:55]
	v_pk_fma_f32 v[54:55], v[126:127], v[6:7], v[4:5]
	v_pk_add_f32 v[30:31], v[30:31], v[72:73] op_sel_hi:[1,0] neg_lo:[0,1] neg_hi:[0,1]
	v_add_f32_e32 v4, 0, v54
	v_add_f32_e32 v4, v4, v55
	v_pk_mul_f32 v[30:31], v[72:73], v[30:31] op_sel:[1,0]
	v_pk_mul_f32 v[24:25], v[24:25], s[34:35] op_sel_hi:[1,0]
	v_add_f32_e32 v4, v4, v52
	v_pk_add_f32 v[28:29], v[28:29], v[72:73] op_sel_hi:[1,0] neg_lo:[0,1] neg_hi:[0,1]
	v_pk_fma_f32 v[30:31], v[30:31], v[46:47], v[50:51]
	v_pk_fma_f32 v[50:51], v[130:131], v[12:13], v[24:25]
	v_add_f32_e32 v4, v4, v53
	v_pk_mul_f32 v[28:29], v[72:73], v[28:29] op_sel:[1,0]
	v_pk_mul_f32 v[26:27], v[26:27], s[34:35] op_sel_hi:[1,0]
	v_add_f32_e32 v4, v4, v50
	v_pk_fma_f32 v[28:29], v[28:29], v[44:45], v[48:49]
	v_pk_fma_f32 v[48:49], v[132:133], v[14:15], v[26:27]
	v_add_f32_e32 v4, v4, v51
	v_pk_add_f32 v[8:9], v[8:9], 1.0 op_sel_hi:[1,0]
	v_pk_mul_f32 v[28:29], v[28:29], s[34:35] op_sel_hi:[1,0]
	v_add_f32_e32 v4, v4, v48
	v_pk_fma_f32 v[46:47], v[134:135], v[8:9], v[28:29]
	v_add_f32_e32 v4, v4, v49
	v_pk_add_f32 v[10:11], v[10:11], 1.0 op_sel_hi:[1,0]
	v_pk_mul_f32 v[30:31], v[30:31], s[34:35] op_sel_hi:[1,0]
	v_add_f32_e32 v4, v4, v46
	v_pk_fma_f32 v[44:45], v[136:137], v[10:11], v[30:31]
	v_add_f32_e32 v4, v4, v47
	v_add_f32_e32 v4, v4, v44
	v_add_f32_e32 v4, v4, v45
	v_add_f32_e32 v4, v4, v42
	v_add_f32_e32 v4, v4, v43
	v_add_f32_e32 v4, v4, v40
	v_add_f32_e32 v4, v4, v41
	ds_bpermute_b32 v5, v2, v4
	v_cndmask_b32_e32 v6, v178, v74, vcc
	v_lshlrev_b32_e32 v74, 2, v6
	v_xor_b32_e32 v6, 8, v178
	v_cmp_lt_i32_e32 vcc, v6, v142
	s_waitcnt lgkmcnt(0)
	v_add_f32_e32 v4, v4, v5
	ds_bpermute_b32 v5, v1, v4
	v_cndmask_b32_e32 v6, v178, v6, vcc
	v_lshlrev_b32_e32 v75, 2, v6
	v_xor_b32_e32 v6, 16, v178
	v_cmp_lt_i32_e32 vcc, v6, v142
	s_waitcnt lgkmcnt(0)
	v_add_f32_e32 v4, v4, v5
	ds_bpermute_b32 v5, v74, v4
	v_cndmask_b32_e32 v6, v178, v6, vcc
	v_lshlrev_b32_e32 v126, 2, v6
	v_xor_b32_e32 v6, 32, v178
	v_cmp_lt_i32_e32 vcc, v6, v142
	s_waitcnt lgkmcnt(0)
	v_add_f32_e32 v7, v4, v5
	ds_bpermute_b32 v8, v75, v7
	v_cndmask_b32_e32 v4, v178, v6, vcc
	v_lshlrev_b32_e32 v127, 2, v4
	v_lshl_add_u64 v[4:5], s[12:13], 0, v[22:23]
	v_lshl_add_u64 v[36:37], s[90:91], 0, v[22:23]
	s_waitcnt lgkmcnt(0)
	v_add_f32_e32 v24, v7, v8
	ds_bpermute_b32 v25, v126, v24
	ds_read_b128 v[16:19], v185 offset:11264
	global_load_dword v184, v187, s[12:13]
	ds_read_b128 v[12:15], v185 offset:10240
	global_load_dword v184, v187, s[12:13]
	ds_read_b128 v[8:11], v185 offset:9216
	global_load_dword v184, v187, s[12:13]
	s_nop 0
	ds_read_b128 v[4:7], v185 offset:8192
	global_load_dword v184, v187, s[12:13]
	v_lshl_add_u64 v[22:23], s[0:1], 0, v[22:23]
	v_readlane_b32 s0, v255, 23
	v_readlane_b32 s1, v255, 24
	s_waitcnt lgkmcnt(0)
	v_add_f32_e32 v56, v24, v25
	ds_read_b128 v[24:27], v185 offset:15360
	global_load_dword v184, v187, s[90:91]
	ds_read_b128 v[28:31], v185 offset:14336
	global_load_dword v184, v187, s[90:91]
	ds_read_b128 v[32:35], v185 offset:13312
	global_load_dword v184, v187, s[90:91]
	s_nop 0
	ds_read_b128 v[36:39], v185 offset:12288
	global_load_dword v184, v187, s[90:91]
	ds_bpermute_b32 v57, v127, v56
	s_waitcnt lgkmcnt(0)
	v_add_f32_e32 v56, v56, v57
	v_mul_f32_e32 v56, 0x3a800000, v56
	v_pk_add_f32 v[54:55], v[54:55], v[56:57] op_sel_hi:[1,0] neg_lo:[0,1] neg_hi:[0,1]
	v_pk_add_f32 v[52:53], v[52:53], v[56:57] op_sel_hi:[1,0] neg_lo:[0,1] neg_hi:[0,1]
	v_pk_mul_f32 v[58:59], v[54:55], v[54:55]
	v_pk_mul_f32 v[60:61], v[52:53], v[52:53]
	v_add_f32_e32 v58, v58, v59
	v_pk_add_f32 v[50:51], v[50:51], v[56:57] op_sel_hi:[1,0] neg_lo:[0,1] neg_hi:[0,1]
	v_add_f32_e32 v58, v60, v58
	v_pk_mul_f32 v[62:63], v[50:51], v[50:51]
	v_add_f32_e32 v58, v61, v58
	v_pk_add_f32 v[48:49], v[48:49], v[56:57] op_sel_hi:[1,0] neg_lo:[0,1] neg_hi:[0,1]
	v_add_f32_e32 v58, v62, v58
	v_pk_mul_f32 v[64:65], v[48:49], v[48:49]
	v_add_f32_e32 v58, v63, v58
	v_pk_add_f32 v[46:47], v[46:47], v[56:57] op_sel_hi:[1,0] neg_lo:[0,1] neg_hi:[0,1]
	v_add_f32_e32 v58, v64, v58
	v_pk_mul_f32 v[66:67], v[46:47], v[46:47]
	v_add_f32_e32 v58, v65, v58
	v_pk_add_f32 v[44:45], v[44:45], v[56:57] op_sel_hi:[1,0] neg_lo:[0,1] neg_hi:[0,1]
	v_add_f32_e32 v58, v66, v58
	v_pk_mul_f32 v[68:69], v[44:45], v[44:45]
	v_add_f32_e32 v58, v67, v58
	v_pk_add_f32 v[42:43], v[42:43], v[56:57] op_sel_hi:[1,0] neg_lo:[0,1] neg_hi:[0,1]
	v_add_f32_e32 v58, v68, v58
	v_pk_mul_f32 v[70:71], v[42:43], v[42:43]
	v_add_f32_e32 v58, v69, v58
	v_pk_add_f32 v[40:41], v[40:41], v[56:57] op_sel_hi:[1,0] neg_lo:[0,1] neg_hi:[0,1]
	v_add_f32_e32 v58, v70, v58
	v_pk_mul_f32 v[56:57], v[40:41], v[40:41]
	v_add_f32_e32 v58, v71, v58
	v_add_f32_e32 v56, v56, v58
	v_add_f32_e32 v56, v57, v56
	ds_bpermute_b32 v57, v2, v56
	s_waitcnt lgkmcnt(0)
	v_add_f32_e32 v56, v56, v57
	ds_bpermute_b32 v57, v1, v56
	s_waitcnt lgkmcnt(0)
	v_add_f32_e32 v56, v56, v57
	ds_bpermute_b32 v57, v74, v56
	s_waitcnt lgkmcnt(0)
	v_add_f32_e32 v56, v56, v57
	ds_bpermute_b32 v57, v75, v56
	s_waitcnt lgkmcnt(0)
	v_add_f32_e32 v56, v56, v57
	ds_bpermute_b32 v57, v126, v56
	s_waitcnt lgkmcnt(0)
	v_add_f32_e32 v56, v56, v57
	ds_bpermute_b32 v57, v127, v56
	s_waitcnt lgkmcnt(0)
	v_add_f32_e32 v56, v56, v57
	v_fmamk_f32 v56, v56, 0x3a800000, v204
	v_mul_f32_e32 v57, 0x4b800000, v56
	v_cmp_gt_f32_e32 vcc, s22, v56
	s_nop 1
	v_cndmask_b32_e32 v56, v56, v57, vcc
	v_rsq_f32_e32 v56, v56
	s_nop 0
	v_mul_f32_e32 v57, 0x45800000, v56
	v_cndmask_b32_e32 v56, v56, v57, vcc
	v_pk_mul_f32 v[54:55], v[54:55], v[56:57] op_sel_hi:[1,0]
	v_pk_mul_f32 v[52:53], v[52:53], v[56:57] op_sel_hi:[1,0]
	s_waitcnt lgkmcnt(0)
	s_waitcnt vmcnt(0)
	v_pk_fma_f32 v[4:5], v[4:5], v[54:55], v[36:37]
	v_pk_mul_f32 v[36:37], v[50:51], v[56:57] op_sel_hi:[1,0]
	v_pk_fma_f32 v[6:7], v[6:7], v[52:53], v[38:39]
	v_pk_fma_f32 v[8:9], v[8:9], v[36:37], v[32:33]
	v_pk_mul_f32 v[32:33], v[48:49], v[56:57] op_sel_hi:[1,0]
	s_and_b64 vcc, exec, s[0:1]
	v_pk_fma_f32 v[10:11], v[10:11], v[32:33], v[34:35]
	v_pk_mul_f32 v[32:33], v[46:47], v[56:57] op_sel_hi:[1,0]
	s_nop 0
	v_pk_fma_f32 v[12:13], v[12:13], v[32:33], v[28:29]
	v_pk_mul_f32 v[28:29], v[44:45], v[56:57] op_sel_hi:[1,0]
	s_nop 0
	v_pk_fma_f32 v[14:15], v[14:15], v[28:29], v[30:31]
	v_pk_mul_f32 v[28:29], v[42:43], v[56:57] op_sel_hi:[1,0]
	s_nop 0
	v_pk_fma_f32 v[16:17], v[16:17], v[28:29], v[24:25]
	v_pk_mul_f32 v[24:25], v[40:41], v[56:57] op_sel_hi:[1,0]
	s_nop 0
	v_pk_fma_f32 v[18:19], v[18:19], v[24:25], v[26:27]
	global_store_dwordx4 v[22:23], v[4:7], off
	global_store_dwordx4 v[22:23], v[8:11], off offset:16
	global_store_dwordx4 v[22:23], v[12:15], off offset:32
	global_store_dwordx4 v[22:23], v[16:19], off offset:48
	s_cbranch_vccz .LBB0_977
	s_lshl_b64 s[0:1], s[96:97], 10
	s_mul_hi_i32 s3, s2, 0x6000
	s_mulk_i32 s2, 0x6000
	s_add_u32 s2, s70, s2
	s_addc_u32 s3, s71, s3
	v_lshl_add_u64 v[50:51], v[20:21], 2, s[2:3]
	s_mov_b64 s[2:3], 0x19000
	v_add_co_u32_e32 v34, vcc, s86, v50
	v_lshl_add_u64 v[30:31], v[50:51], 0, s[2:3]
	s_mov_b64 s[2:3], 0x18000
	v_addc_co_u32_e32 v35, vcc, 0, v51, vcc
	v_lshl_add_u64 v[46:47], v[50:51], 0, s[2:3]
	v_add_co_u32_e32 v50, vcc, s67, v50
	global_load_dwordx4 v[22:25], v[30:31], off offset:32
	global_load_dwordx4 v[26:29], v[30:31], off offset:16
	v_addc_co_u32_e32 v51, vcc, 0, v51, vcc
	global_load_dwordx4 v[30:33], v[30:31], off offset:48
	s_nop 0
	global_load_dwordx4 v[34:37], v[34:35], off
	s_nop 0
	ds_read_b128 v[38:41], v188 offset:5120
	global_load_dword v184, v187, s[70:71]
	ds_read_b128 v[42:45], v188 offset:7168
	global_load_dword v184, v187, s[70:71]
	s_nop 0
	ds_read_b128 v[46:49], v188 offset:6144
	global_load_dword v184, v187, s[70:71]
	s_lshl_b64 s[0:1], s[0:1], 1
	ds_read_b128 v[50:53], v188 offset:4096
	global_load_dword v184, v187, s[70:71]
	s_add_u32 s0, s76, s0
	s_addc_u32 s1, s77, s1
	v_lshl_add_u64 v[20:21], v[20:21], 1, s[0:1]
	s_waitcnt lgkmcnt(0)
	s_waitcnt vmcnt(7)
	v_pk_add_f32 v[22:23], v[22:23], 1.0 op_sel_hi:[1,0]
	s_waitcnt lgkmcnt(0)
	s_waitcnt vmcnt(6)
	v_pk_add_f32 v[26:27], v[26:27], 1.0 op_sel_hi:[1,0]
	v_pk_add_f32 v[28:29], v[28:29], 1.0 op_sel_hi:[1,0]
	s_waitcnt lgkmcnt(0)
	s_waitcnt vmcnt(4)
	v_pk_add_f32 v[34:35], v[34:35], 1.0 op_sel_hi:[1,0]
	v_pk_add_f32 v[36:37], v[36:37], 1.0 op_sel_hi:[1,0]
	v_pk_add_f32 v[24:25], v[24:25], 1.0 op_sel_hi:[1,0]
	v_pk_add_f32 v[30:31], v[30:31], 1.0 op_sel_hi:[1,0]
	v_pk_add_f32 v[32:33], v[32:33], 1.0 op_sel_hi:[1,0]
	s_waitcnt lgkmcnt(0)
	s_waitcnt vmcnt(3)
	v_pk_fma_f32 v[8:9], v[8:9], v[26:27], v[38:39]
	v_pk_fma_f32 v[10:11], v[10:11], v[28:29], v[40:41]
	s_waitcnt lgkmcnt(0)
	s_waitcnt vmcnt(1)
	v_pk_fma_f32 v[12:13], v[12:13], v[22:23], v[46:47]
	s_waitcnt lgkmcnt(0)
	s_waitcnt vmcnt(0)
	v_pk_fma_f32 v[4:5], v[4:5], v[34:35], v[50:51]
	v_pk_fma_f32 v[22:23], v[6:7], v[36:37], v[52:53]
	v_pk_fma_f32 v[14:15], v[14:15], v[24:25], v[48:49]
	v_pk_fma_f32 v[16:17], v[16:17], v[30:31], v[42:43]
	v_pk_fma_f32 v[18:19], v[18:19], v[32:33], v[44:45]
	v_cvt_pk_bf16_f32 v6, v8, v9
	v_cvt_pk_bf16_f32 v7, v10, v11
	v_cvt_pk_bf16_f32 v4, v4, v5
	v_cvt_pk_bf16_f32 v5, v22, v23
	v_cvt_pk_bf16_f32 v8, v12, v13
	v_cvt_pk_bf16_f32 v9, v14, v15
	v_cvt_pk_bf16_f32 v10, v16, v17
	v_cvt_pk_bf16_f32 v11, v18, v19
	global_store_dwordx4 v[20:21], v[4:7], off
	global_store_dwordx4 v[20:21], v[8:11], off offset:16
.LBB0_977:
	s_or_b32 s22, s96, 1
	s_add_i32 s0, s22, s35
	s_ashr_i32 s1, s0, 31
	s_lshr_b32 s1, s1, 19
	s_add_i32 s0, s0, s1
	s_ashr_i32 s2, s0, 13
	s_ashr_i32 s0, s2, 31
	s_add_u32 s1, s2, s87
	s_addc_u32 s0, s0, 0
	s_mulk_i32 s0, 0x6000
	s_mul_hi_u32 s3, s1, 0x6000
	v_mov_b32_e32 v4, v179
	s_add_i32 s3, s3, s0
	s_mulk_i32 s1, 0x6000
	s_add_u32 s0, s70, s1
	v_lshlrev_b32_e32 v20, 4, v4
	s_addc_u32 s1, s71, s3
	s_ashr_i32 s23, s22, 31
	v_readlane_b32 s36, v253, 60
	v_ashrrev_i32_e32 v21, 31, v20
	s_lshl_b64 s[26:27], s[22:23], 12
	v_readlane_b32 s38, v253, 62
	v_lshlrev_b64 v[4:5], 2, v[20:21]
	v_readlane_b32 s39, v253, 63
	s_add_u32 s6, s38, s26
	v_lshl_add_u64 v[22:23], s[0:1], 0, v[4:5]
	s_mov_b64 s[0:1], 0x5000
	s_addc_u32 s7, s39, s27
	v_lshl_add_u64 v[14:15], v[22:23], 0, s[0:1]
	s_lshl_b64 s[0:1], s[22:23], 3
	v_add_co_u32_e32 v22, vcc, s18, v22
	s_add_u32 s0, s64, s0
	s_nop 0
	v_addc_co_u32_e32 v23, vcc, 0, v23, vcc
	v_lshl_add_u64 v[18:19], s[6:7], 0, v[4:5]
	s_addc_u32 s1, s65, s1
	ds_read_b128 v[6:9], v188 offset:3072
	global_load_dword v184, v187, s[70:71]
	ds_read_b128 v[10:13], v188 offset:2048
	global_load_dword v184, v187, s[70:71]
	s_nop 0
	ds_read_b128 v[14:17], v188 offset:1024
	global_load_dword v184, v187, s[70:71]
	s_nop 0
	ds_read_b128 v[22:25], v188 offset:0
	global_load_dword v184, v187, s[70:71]
	s_nop 0
	global_load_dwordx2 v[128:129], v3, s[0:1]
	global_load_dwordx4 v[26:29], v[18:19], off
	global_load_dwordx4 v[30:33], v[18:19], off offset:16
	global_load_dwordx4 v[34:37], v[18:19], off offset:32
	global_load_dwordx4 v[38:41], v[18:19], off offset:48
	v_lshl_add_u64 v[70:71], s[28:29], 0, v[4:5]
	v_lshl_add_u64 v[18:19], s[16:17], 0, v[4:5]
	ds_read_b128 v[42:45], v185 offset:7168
	global_load_dword v184, v187, s[28:29]
	ds_read_b128 v[46:49], v185 offset:3072
	global_load_dword v184, v187, s[16:17]
	ds_read_b128 v[50:53], v185 offset:2048
	global_load_dword v184, v187, s[16:17]
	ds_read_b128 v[54:57], v185 offset:6144
	global_load_dword v184, v187, s[28:29]
	ds_read_b128 v[58:61], v185 offset:5120
	global_load_dword v184, v187, s[28:29]
	ds_read_b128 v[62:65], v185 offset:1024
	global_load_dword v184, v187, s[16:17]
	ds_read_b128 v[66:69], v185 offset:0
	global_load_dword v184, v187, s[16:17]
	s_nop 0
	ds_read_b128 v[70:73], v185 offset:4096
	global_load_dword v184, v187, s[28:29]
	v_readlane_b32 s37, v253, 61
	v_readlane_b32 s36, v255, 42
	v_readlane_b32 s24, v255, 23
	v_readlane_b32 s38, v255, 44
	v_readlane_b32 s25, v255, 24
	s_add_u32 s20, s30, s26
	s_addc_u32 s21, s31, s27
	s_andn2_b64 vcc, exec, s[24:25]
	v_readlane_b32 s40, v254, 0
	v_readlane_b32 s41, v254, 1
	v_readlane_b32 s42, v254, 2
	v_readlane_b32 s43, v254, 3
	v_readlane_b32 s44, v254, 4
	v_readlane_b32 s45, v254, 5
	v_readlane_b32 s46, v254, 6
	v_readlane_b32 s47, v254, 7
	v_readlane_b32 s48, v254, 8
	v_readlane_b32 s49, v254, 9
	v_readlane_b32 s50, v254, 10
	v_readlane_b32 s51, v254, 11
	v_readlane_b32 s37, v255, 43
	v_readlane_b32 s39, v255, 45
	s_waitcnt lgkmcnt(0)
	s_waitcnt vmcnt(13)
	v_pk_add_f32 v[18:19], v[24:25], 1.0 op_sel_hi:[1,0]
	v_pk_add_f32 v[22:23], v[22:23], 1.0 op_sel_hi:[1,0]
	s_waitcnt lgkmcnt(0)
	s_waitcnt vmcnt(11)
	v_pk_add_f32 v[24:25], v[26:27], v[128:129] op_sel_hi:[1,0] neg_lo:[0,1] neg_hi:[0,1]
	v_pk_add_f32 v[26:27], v[28:29], v[128:129] op_sel_hi:[1,0] neg_lo:[0,1] neg_hi:[0,1]
	s_waitcnt lgkmcnt(0)
	s_waitcnt vmcnt(10)
	v_pk_add_f32 v[28:29], v[30:31], v[128:129] op_sel_hi:[1,0] neg_lo:[0,1] neg_hi:[0,1]
	v_pk_add_f32 v[30:31], v[32:33], v[128:129] op_sel_hi:[1,0] neg_lo:[0,1] neg_hi:[0,1]
	s_waitcnt lgkmcnt(0)
	s_waitcnt vmcnt(9)
	v_pk_add_f32 v[32:33], v[34:35], v[128:129] op_sel_hi:[1,0] neg_lo:[0,1] neg_hi:[0,1]
	v_pk_add_f32 v[34:35], v[36:37], v[128:129] op_sel_hi:[1,0] neg_lo:[0,1] neg_hi:[0,1]
	s_waitcnt lgkmcnt(0)
	s_waitcnt vmcnt(8)
	v_pk_add_f32 v[36:37], v[38:39], v[128:129] op_sel_hi:[1,0] neg_lo:[0,1] neg_hi:[0,1]
	v_pk_add_f32 v[38:39], v[40:41], v[128:129] op_sel_hi:[1,0] neg_lo:[0,1] neg_hi:[0,1]
	v_pk_mul_f32 v[24:25], v[128:129], v[24:25] op_sel:[1,0]
	v_pk_mul_f32 v[38:39], v[128:129], v[38:39] op_sel:[1,0]
	s_waitcnt lgkmcnt(0)
	s_waitcnt vmcnt(0)
	v_pk_fma_f32 v[24:25], v[66:67], v[24:25], v[70:71]
	v_pk_mul_f32 v[32:33], v[128:129], v[32:33] op_sel:[1,0]
	v_pk_mul_f32 v[26:27], v[128:129], v[26:27] op_sel:[1,0]
	v_pk_fma_f32 v[38:39], v[38:39], v[48:49], v[44:45]
	v_pk_mul_f32 v[24:25], v[24:25], s[34:35] op_sel_hi:[1,0]
	v_pk_add_f32 v[8:9], v[8:9], 1.0 op_sel_hi:[1,0]
	v_pk_mul_f32 v[36:37], v[128:129], v[36:37] op_sel:[1,0]
	v_pk_fma_f32 v[32:33], v[32:33], v[50:51], v[54:55]
	v_pk_fma_f32 v[26:27], v[26:27], v[68:69], v[72:73]
	v_pk_mul_f32 v[38:39], v[38:39], s[34:35] op_sel_hi:[1,0]
	v_pk_fma_f32 v[54:55], v[110:111], v[22:23], v[24:25]
	v_pk_mul_f32 v[34:35], v[128:129], v[34:35] op_sel:[1,0]
	v_pk_mul_f32 v[28:29], v[128:129], v[28:29] op_sel:[1,0]
	v_pk_fma_f32 v[36:37], v[36:37], v[46:47], v[42:43]
	v_pk_mul_f32 v[26:27], v[26:27], s[34:35] op_sel_hi:[1,0]
	v_pk_fma_f32 v[42:43], v[124:125], v[8:9], v[38:39]
	v_add_f32_e32 v8, 0, v54
	v_pk_fma_f32 v[34:35], v[34:35], v[52:53], v[56:57]
	v_pk_fma_f32 v[28:29], v[28:29], v[62:63], v[58:59]
	v_pk_fma_f32 v[52:53], v[112:113], v[18:19], v[26:27]
	v_add_f32_e32 v8, v8, v55
	v_pk_add_f32 v[14:15], v[14:15], 1.0 op_sel_hi:[1,0]
	v_pk_mul_f32 v[30:31], v[128:129], v[30:31] op_sel:[1,0]
	v_pk_mul_f32 v[28:29], v[28:29], s[34:35] op_sel_hi:[1,0]
	v_add_f32_e32 v8, v8, v52
	v_pk_fma_f32 v[30:31], v[30:31], v[64:65], v[60:61]
	v_pk_fma_f32 v[50:51], v[114:115], v[14:15], v[28:29]
	v_add_f32_e32 v8, v8, v53
	v_pk_add_f32 v[16:17], v[16:17], 1.0 op_sel_hi:[1,0]
	v_pk_mul_f32 v[30:31], v[30:31], s[34:35] op_sel_hi:[1,0]
	v_add_f32_e32 v8, v8, v50
	v_pk_fma_f32 v[48:49], v[116:117], v[16:17], v[30:31]
	v_add_f32_e32 v8, v8, v51
	v_pk_add_f32 v[10:11], v[10:11], 1.0 op_sel_hi:[1,0]
	v_pk_mul_f32 v[32:33], v[32:33], s[34:35] op_sel_hi:[1,0]
	v_add_f32_e32 v8, v8, v48
	v_pk_fma_f32 v[46:47], v[118:119], v[10:11], v[32:33]
	v_add_f32_e32 v8, v8, v49
	v_pk_add_f32 v[12:13], v[12:13], 1.0 op_sel_hi:[1,0]
	v_pk_mul_f32 v[34:35], v[34:35], s[34:35] op_sel_hi:[1,0]
	v_add_f32_e32 v8, v8, v46
	v_pk_fma_f32 v[44:45], v[120:121], v[12:13], v[34:35]
	v_add_f32_e32 v8, v8, v47
	v_pk_add_f32 v[6:7], v[6:7], 1.0 op_sel_hi:[1,0]
	v_pk_mul_f32 v[36:37], v[36:37], s[34:35] op_sel_hi:[1,0]
	v_add_f32_e32 v8, v8, v44
	v_pk_fma_f32 v[6:7], v[122:123], v[6:7], v[36:37]
	v_add_f32_e32 v8, v8, v45
	v_add_f32_e32 v8, v8, v6
	v_add_f32_e32 v8, v8, v7
	v_add_f32_e32 v8, v8, v42
	v_add_f32_e32 v8, v8, v43
	ds_bpermute_b32 v9, v2, v8
	v_lshl_add_u64 v[22:23], s[12:13], 0, v[4:5]
	v_lshl_add_u64 v[38:39], s[90:91], 0, v[4:5]
	s_waitcnt lgkmcnt(0)
	v_add_f32_e32 v8, v8, v9
	ds_bpermute_b32 v9, v1, v8
	s_waitcnt lgkmcnt(0)
	v_add_f32_e32 v8, v8, v9
	ds_bpermute_b32 v9, v74, v8
	s_waitcnt lgkmcnt(0)
	v_add_f32_e32 v8, v8, v9
	ds_bpermute_b32 v9, v75, v8
	s_waitcnt lgkmcnt(0)
	v_add_f32_e32 v26, v8, v9
	ds_bpermute_b32 v27, v126, v26
	ds_read_b128 v[8:11], v185 offset:11264
	global_load_dword v184, v187, s[12:13]
	ds_read_b128 v[12:15], v185 offset:10240
	global_load_dword v184, v187, s[12:13]
	ds_read_b128 v[16:19], v185 offset:9216
	global_load_dword v184, v187, s[12:13]
	s_nop 0
	ds_read_b128 v[22:25], v185 offset:8192
	global_load_dword v184, v187, s[12:13]
	s_waitcnt lgkmcnt(0)
	v_add_f32_e32 v56, v26, v27
	ds_read_b128 v[26:29], v185 offset:15360
	global_load_dword v184, v187, s[90:91]
	ds_read_b128 v[30:33], v185 offset:14336
	global_load_dword v184, v187, s[90:91]
	ds_read_b128 v[34:37], v185 offset:13312
	global_load_dword v184, v187, s[90:91]
	s_nop 0
	ds_read_b128 v[38:41], v185 offset:12288
	global_load_dword v184, v187, s[90:91]
	ds_bpermute_b32 v57, v127, v56
	s_waitcnt lgkmcnt(0)
	v_add_f32_e32 v56, v56, v57
	v_mul_f32_e32 v56, 0x3a800000, v56
	v_pk_add_f32 v[54:55], v[54:55], v[56:57] op_sel_hi:[1,0] neg_lo:[0,1] neg_hi:[0,1]
	v_pk_add_f32 v[52:53], v[52:53], v[56:57] op_sel_hi:[1,0] neg_lo:[0,1] neg_hi:[0,1]
	v_pk_add_f32 v[50:51], v[50:51], v[56:57] op_sel_hi:[1,0] neg_lo:[0,1] neg_hi:[0,1]
	v_pk_add_f32 v[48:49], v[48:49], v[56:57] op_sel_hi:[1,0] neg_lo:[0,1] neg_hi:[0,1]
	v_pk_add_f32 v[46:47], v[46:47], v[56:57] op_sel_hi:[1,0] neg_lo:[0,1] neg_hi:[0,1]
	v_pk_add_f32 v[44:45], v[44:45], v[56:57] op_sel_hi:[1,0] neg_lo:[0,1] neg_hi:[0,1]
	v_pk_add_f32 v[6:7], v[6:7], v[56:57] op_sel_hi:[1,0] neg_lo:[0,1] neg_hi:[0,1]
	v_pk_add_f32 v[42:43], v[42:43], v[56:57] op_sel_hi:[1,0] neg_lo:[0,1] neg_hi:[0,1]
	v_pk_mul_f32 v[56:57], v[54:55], v[54:55]
	v_pk_mul_f32 v[58:59], v[52:53], v[52:53]
	v_add_f32_e32 v56, v56, v57
	v_add_f32_e32 v56, v58, v56
	v_pk_mul_f32 v[60:61], v[50:51], v[50:51]
	v_add_f32_e32 v56, v59, v56
	v_add_f32_e32 v56, v60, v56
	v_pk_mul_f32 v[62:63], v[48:49], v[48:49]
	v_add_f32_e32 v56, v61, v56
	v_add_f32_e32 v56, v62, v56
	v_pk_mul_f32 v[64:65], v[46:47], v[46:47]
	v_add_f32_e32 v56, v63, v56
	v_add_f32_e32 v56, v64, v56
	v_pk_mul_f32 v[66:67], v[44:45], v[44:45]
	v_add_f32_e32 v56, v65, v56
	v_add_f32_e32 v56, v66, v56
	v_pk_mul_f32 v[68:69], v[6:7], v[6:7]
	v_add_f32_e32 v56, v67, v56
	v_add_f32_e32 v56, v68, v56
	v_pk_mul_f32 v[70:71], v[42:43], v[42:43]
	v_add_f32_e32 v56, v69, v56
	v_add_f32_e32 v56, v70, v56
	v_add_f32_e32 v56, v71, v56
	ds_bpermute_b32 v57, v2, v56
	v_cndmask_b32_e64 v58, 0, 1, s[24:25]
	v_cmp_ne_u32_e64 s[6:7], 1, v58
	s_waitcnt lgkmcnt(0)
	v_add_f32_e32 v56, v56, v57
	ds_bpermute_b32 v57, v1, v56
	s_waitcnt lgkmcnt(0)
	v_add_f32_e32 v56, v56, v57
	ds_bpermute_b32 v57, v74, v56
	s_waitcnt lgkmcnt(0)
	v_add_f32_e32 v56, v56, v57
	ds_bpermute_b32 v57, v75, v56
	s_waitcnt lgkmcnt(0)
	v_add_f32_e32 v56, v56, v57
	ds_bpermute_b32 v57, v126, v56
	s_waitcnt lgkmcnt(0)
	v_add_f32_e32 v56, v56, v57
	ds_bpermute_b32 v57, v127, v56
	s_waitcnt lgkmcnt(0)
	v_add_f32_e32 v56, v56, v57
	v_fmamk_f32 v56, v56, 0x3a800000, v204
	v_mul_f32_e32 v57, 0x4b800000, v56
	v_cmp_gt_f32_e64 s[0:1], s38, v56
	s_nop 1
	v_cndmask_b32_e64 v56, v56, v57, s[0:1]
	v_rsq_f32_e32 v58, v56
	v_lshl_add_u64 v[56:57], s[20:21], 0, v[4:5]
	v_mul_f32_e32 v4, 0x45800000, v58
	v_cndmask_b32_e64 v4, v58, v4, s[0:1]
	v_pk_mul_f32 v[54:55], v[54:55], v[4:5] op_sel_hi:[1,0]
	v_pk_mul_f32 v[52:53], v[52:53], v[4:5] op_sel_hi:[1,0]
	v_pk_mul_f32 v[50:51], v[50:51], v[4:5] op_sel_hi:[1,0]
	v_pk_mul_f32 v[48:49], v[48:49], v[4:5] op_sel_hi:[1,0]
	v_pk_mul_f32 v[46:47], v[46:47], v[4:5] op_sel_hi:[1,0]
	v_pk_mul_f32 v[44:45], v[44:45], v[4:5] op_sel_hi:[1,0]
	v_pk_mul_f32 v[58:59], v[6:7], v[4:5] op_sel_hi:[1,0]
	v_pk_mul_f32 v[42:43], v[42:43], v[4:5] op_sel_hi:[1,0]
	s_waitcnt lgkmcnt(0)
	s_waitcnt vmcnt(0)
	v_pk_fma_f32 v[4:5], v[22:23], v[54:55], v[38:39]
	v_pk_fma_f32 v[6:7], v[24:25], v[52:53], v[40:41]
	v_pk_fma_f32 v[16:17], v[16:17], v[50:51], v[34:35]
	v_pk_fma_f32 v[18:19], v[18:19], v[48:49], v[36:37]
	v_pk_fma_f32 v[12:13], v[12:13], v[46:47], v[30:31]
	v_pk_fma_f32 v[14:15], v[14:15], v[44:45], v[32:33]
	v_pk_fma_f32 v[8:9], v[8:9], v[58:59], v[26:27]
	v_pk_fma_f32 v[10:11], v[10:11], v[42:43], v[28:29]
	global_store_dwordx4 v[56:57], v[4:7], off
	global_store_dwordx4 v[56:57], v[16:19], off offset:16
	global_store_dwordx4 v[56:57], v[12:15], off offset:32
	global_store_dwordx4 v[56:57], v[8:11], off offset:48
	s_cbranch_vccnz .LBB0_979
	s_lshl_b64 s[0:1], s[22:23], 10
	s_mul_hi_i32 s3, s2, 0x6000
	s_mulk_i32 s2, 0x6000
	s_add_u32 s2, s70, s2
	s_addc_u32 s3, s71, s3
	v_lshl_add_u64 v[50:51], v[20:21], 2, s[2:3]
	s_mov_b64 s[2:3], 0x19000
	v_add_co_u32_e32 v34, vcc, s86, v50
	v_lshl_add_u64 v[30:31], v[50:51], 0, s[2:3]
	s_mov_b64 s[2:3], 0x18000
	v_addc_co_u32_e32 v35, vcc, 0, v51, vcc
	v_lshl_add_u64 v[46:47], v[50:51], 0, s[2:3]
	v_add_co_u32_e32 v50, vcc, s67, v50
	global_load_dwordx4 v[22:25], v[30:31], off offset:32
	global_load_dwordx4 v[26:29], v[30:31], off offset:16
	v_addc_co_u32_e32 v51, vcc, 0, v51, vcc
	global_load_dwordx4 v[30:33], v[30:31], off offset:48
	s_nop 0
	global_load_dwordx4 v[34:37], v[34:35], off
	s_nop 0
	ds_read_b128 v[38:41], v188 offset:5120
	global_load_dword v184, v187, s[70:71]
	ds_read_b128 v[42:45], v188 offset:7168
	global_load_dword v184, v187, s[70:71]
	s_nop 0
	ds_read_b128 v[46:49], v188 offset:6144
	global_load_dword v184, v187, s[70:71]
	s_lshl_b64 s[0:1], s[0:1], 1
	ds_read_b128 v[50:53], v188 offset:4096
	global_load_dword v184, v187, s[70:71]
	s_add_u32 s0, s76, s0
	s_addc_u32 s1, s77, s1
	v_lshl_add_u64 v[20:21], v[20:21], 1, s[0:1]
	s_waitcnt lgkmcnt(0)
	s_waitcnt vmcnt(7)
	v_pk_add_f32 v[22:23], v[22:23], 1.0 op_sel_hi:[1,0]
	s_waitcnt lgkmcnt(0)
	s_waitcnt vmcnt(6)
	v_pk_add_f32 v[26:27], v[26:27], 1.0 op_sel_hi:[1,0]
	v_pk_add_f32 v[28:29], v[28:29], 1.0 op_sel_hi:[1,0]
	s_waitcnt lgkmcnt(0)
	s_waitcnt vmcnt(4)
	v_pk_add_f32 v[34:35], v[34:35], 1.0 op_sel_hi:[1,0]
	v_pk_add_f32 v[36:37], v[36:37], 1.0 op_sel_hi:[1,0]
	v_pk_add_f32 v[24:25], v[24:25], 1.0 op_sel_hi:[1,0]
	v_pk_add_f32 v[30:31], v[30:31], 1.0 op_sel_hi:[1,0]
	v_pk_add_f32 v[32:33], v[32:33], 1.0 op_sel_hi:[1,0]
	s_waitcnt lgkmcnt(0)
	s_waitcnt vmcnt(3)
	v_pk_fma_f32 v[16:17], v[16:17], v[26:27], v[38:39]
	v_pk_fma_f32 v[18:19], v[18:19], v[28:29], v[40:41]
	s_waitcnt lgkmcnt(0)
	s_waitcnt vmcnt(0)
	v_pk_fma_f32 v[4:5], v[4:5], v[34:35], v[50:51]
	v_pk_fma_f32 v[26:27], v[6:7], v[36:37], v[52:53]
	v_pk_fma_f32 v[12:13], v[12:13], v[22:23], v[46:47]
	v_pk_fma_f32 v[14:15], v[14:15], v[24:25], v[48:49]
	v_pk_fma_f32 v[22:23], v[8:9], v[30:31], v[42:43]
	v_pk_fma_f32 v[24:25], v[10:11], v[32:33], v[44:45]
	v_cvt_pk_bf16_f32 v6, v16, v17
	v_cvt_pk_bf16_f32 v7, v18, v19
	v_cvt_pk_bf16_f32 v4, v4, v5
	v_cvt_pk_bf16_f32 v5, v26, v27
	v_cvt_pk_bf16_f32 v8, v12, v13
	v_cvt_pk_bf16_f32 v9, v14, v15
	v_cvt_pk_bf16_f32 v10, v22, v23
	v_cvt_pk_bf16_f32 v11, v24, v25
	global_store_dwordx4 v[20:21], v[4:7], off
	global_store_dwordx4 v[20:21], v[8:11], off offset:16
.LBB0_979:
	s_or_b32 s0, s96, 2
	s_add_i32 s1, s0, s35
	s_ashr_i32 s2, s1, 31
	s_lshr_b32 s2, s2, 19
	s_add_i32 s1, s1, s2
	s_ashr_i32 s2, s1, 13
	s_ashr_i32 s1, s2, 31
	s_add_u32 s3, s2, s87
	s_addc_u32 s1, s1, 0
	s_mulk_i32 s1, 0x6000
	s_mul_hi_u32 s20, s3, 0x6000
	v_mov_b32_e32 v4, v179
	s_add_i32 s1, s20, s1
	s_mulk_i32 s3, 0x6000
	s_add_u32 s20, s70, s3
	v_lshlrev_b32_e32 v52, 4, v4
	s_addc_u32 s21, s71, s1
	s_ashr_i32 s1, s0, 31
	v_readlane_b32 s36, v253, 60
	v_ashrrev_i32_e32 v53, 31, v52
	s_lshl_b64 s[22:23], s[0:1], 12
	v_readlane_b32 s38, v253, 62
	v_lshlrev_b64 v[54:55], 2, v[52:53]
	v_readlane_b32 s39, v253, 63
	s_add_u32 s24, s38, s22
	v_lshl_add_u64 v[20:21], s[20:21], 0, v[54:55]
	s_mov_b64 s[20:21], 0x5000
	s_addc_u32 s25, s39, s23
	v_lshl_add_u64 v[22:23], v[20:21], 0, s[20:21]
	s_lshl_b64 s[20:21], s[0:1], 3
	s_add_u32 s20, s64, s20
	s_addc_u32 s21, s65, s21
	global_load_dwordx2 v[58:59], v3, s[20:21]
	v_lshl_add_u64 v[16:17], s[24:25], 0, v[54:55]
	global_load_dwordx4 v[4:7], v[16:17], off offset:48
	global_load_dwordx4 v[8:11], v[16:17], off offset:32
	global_load_dwordx4 v[12:15], v[16:17], off offset:16
	s_nop 0
	global_load_dwordx4 v[16:19], v[16:17], off
	v_lshl_add_u64 v[24:25], s[16:17], 0, v[54:55]
	v_lshl_add_u64 v[26:27], s[28:29], 0, v[54:55]
	v_lshl_add_u64 v[32:33], s[90:91], 0, v[54:55]
	v_readlane_b32 s24, v255, 42
	v_readlane_b32 s26, v255, 44
	s_add_u32 s20, s30, s22
	s_addc_u32 s21, s31, s23
	v_readlane_b32 s37, v253, 61
	v_readlane_b32 s40, v254, 0
	v_readlane_b32 s41, v254, 1
	v_readlane_b32 s42, v254, 2
	v_readlane_b32 s43, v254, 3
	v_readlane_b32 s44, v254, 4
	v_readlane_b32 s45, v254, 5
	v_readlane_b32 s46, v254, 6
	v_readlane_b32 s47, v254, 7
	v_readlane_b32 s48, v254, 8
	v_readlane_b32 s49, v254, 9
	v_readlane_b32 s50, v254, 10
	v_readlane_b32 s51, v254, 11
	v_readlane_b32 s25, v255, 43
	v_readlane_b32 s27, v255, 45
	s_waitcnt lgkmcnt(0)
	s_waitcnt vmcnt(3)
	v_pk_add_f32 v[62:63], v[4:5], v[58:59] op_sel_hi:[1,0] neg_lo:[0,1] neg_hi:[0,1]
	v_pk_add_f32 v[4:5], v[6:7], v[58:59] op_sel_hi:[1,0] neg_lo:[0,1] neg_hi:[0,1]
	v_add_co_u32_e32 v6, vcc, s18, v20
	s_waitcnt lgkmcnt(0)
	s_waitcnt vmcnt(1)
	v_pk_add_f32 v[70:71], v[14:15], v[58:59] op_sel_hi:[1,0] neg_lo:[0,1] neg_hi:[0,1]
	v_addc_co_u32_e32 v7, vcc, 0, v21, vcc
	ds_read_b128 v[36:39], v188 offset:0
	global_load_dword v184, v187, s[70:71]
	ds_read_b128 v[110:113], v188 offset:3072
	global_load_dword v184, v187, s[70:71]
	ds_read_b128 v[114:117], v188 offset:2048
	global_load_dword v184, v187, s[70:71]
	ds_read_b128 v[44:47], v188 offset:1024
	global_load_dword v184, v187, s[70:71]
	ds_read_b128 v[118:121], v185 offset:3072
	global_load_dword v184, v187, s[16:17]
	ds_read_b128 v[122:125], v185 offset:2048
	global_load_dword v184, v187, s[16:17]
	ds_read_b128 v[48:51], v185 offset:1024
	global_load_dword v184, v187, s[16:17]
	ds_read_b128 v[40:43], v185 offset:0
	global_load_dword v184, v187, s[16:17]
	ds_read_b128 v[128:131], v185 offset:7168
	global_load_dword v184, v187, s[28:29]
	ds_read_b128 v[132:135], v185 offset:6144
	global_load_dword v184, v187, s[28:29]
	ds_read_b128 v[136:139], v185 offset:5120
	global_load_dword v184, v187, s[28:29]
	ds_read_b128 v[140:143], v185 offset:4096
	global_load_dword v184, v187, s[28:29]
	v_pk_mul_f32 v[70:71], v[58:59], v[70:71] op_sel:[1,0]
	v_pk_add_f32 v[66:67], v[12:13], v[58:59] op_sel_hi:[1,0] neg_lo:[0,1] neg_hi:[0,1]
	s_waitcnt lgkmcnt(0)
	s_waitcnt vmcnt(12)
	v_pk_add_f32 v[64:65], v[18:19], v[58:59] op_sel_hi:[1,0] neg_lo:[0,1] neg_hi:[0,1]
	v_pk_add_f32 v[60:61], v[16:17], v[58:59] op_sel_hi:[1,0] neg_lo:[0,1] neg_hi:[0,1]
	v_pk_mul_f32 v[4:5], v[58:59], v[4:5] op_sel:[1,0]
	v_pk_add_f32 v[68:69], v[10:11], v[58:59] op_sel_hi:[1,0] neg_lo:[0,1] neg_hi:[0,1]
	v_pk_mul_f32 v[62:63], v[58:59], v[62:63] op_sel:[1,0]
	v_pk_add_f32 v[72:73], v[8:9], v[58:59] op_sel_hi:[1,0] neg_lo:[0,1] neg_hi:[0,1]
	v_pk_mul_f32 v[68:69], v[58:59], v[68:69] op_sel:[1,0]
	v_pk_mul_f32 v[72:73], v[58:59], v[72:73] op_sel:[1,0]
	v_lshl_add_u64 v[8:9], s[12:13], 0, v[54:55]
	s_waitcnt lgkmcnt(0)
	s_waitcnt vmcnt(11)
	v_pk_add_f32 v[38:39], v[38:39], 1.0 op_sel_hi:[1,0]
	v_pk_add_f32 v[36:37], v[36:37], 1.0 op_sel_hi:[1,0]
	s_waitcnt lgkmcnt(0)
	s_waitcnt vmcnt(10)
	v_pk_add_f32 v[6:7], v[112:113], 1.0 op_sel_hi:[1,0]
	s_waitcnt lgkmcnt(0)
	s_waitcnt vmcnt(8)
	v_pk_add_f32 v[46:47], v[46:47], 1.0 op_sel_hi:[1,0]
	v_pk_add_f32 v[44:45], v[44:45], 1.0 op_sel_hi:[1,0]
	s_waitcnt lgkmcnt(0)
	s_waitcnt vmcnt(3)
	v_pk_fma_f32 v[4:5], v[4:5], v[120:121], v[130:131]
	s_nop 0
	v_pk_mul_f32 v[4:5], v[4:5], s[34:35] op_sel_hi:[1,0]
	s_waitcnt lgkmcnt(0)
	s_waitcnt vmcnt(1)
	v_pk_fma_f32 v[50:51], v[70:71], v[50:51], v[138:139]
	v_pk_fma_f32 v[62:63], v[62:63], v[118:119], v[128:129]
	v_pk_mul_f32 v[50:51], v[50:51], s[34:35] op_sel_hi:[1,0]
	v_pk_fma_f32 v[56:57], v[108:109], v[6:7], v[4:5]
	v_pk_fma_f32 v[46:47], v[100:101], v[46:47], v[50:51]
	v_pk_mul_f32 v[50:51], v[58:59], v[66:67] op_sel:[1,0]
	v_pk_mul_f32 v[62:63], v[62:63], s[34:35] op_sel_hi:[1,0]
	v_pk_fma_f32 v[48:49], v[50:51], v[48:49], v[136:137]
	v_pk_add_f32 v[108:109], v[110:111], 1.0 op_sel_hi:[1,0]
	v_pk_mul_f32 v[48:49], v[48:49], s[34:35] op_sel_hi:[1,0]
	v_pk_fma_f32 v[68:69], v[68:69], v[124:125], v[134:135]
	v_pk_fma_f32 v[44:45], v[98:99], v[44:45], v[48:49]
	v_pk_mul_f32 v[48:49], v[58:59], v[64:65] op_sel:[1,0]
	v_pk_fma_f32 v[62:63], v[106:107], v[108:109], v[62:63]
	s_waitcnt lgkmcnt(0)
	s_waitcnt vmcnt(0)
	v_pk_fma_f32 v[42:43], v[48:49], v[42:43], v[142:143]
	v_pk_mul_f32 v[68:69], v[68:69], s[34:35] op_sel_hi:[1,0]
	v_pk_mul_f32 v[42:43], v[42:43], s[34:35] op_sel_hi:[1,0]
	v_pk_add_f32 v[106:107], v[116:117], 1.0 op_sel_hi:[1,0]
	v_pk_fma_f32 v[38:39], v[96:97], v[38:39], v[42:43]
	v_pk_mul_f32 v[42:43], v[58:59], v[60:61] op_sel:[1,0]
	v_pk_fma_f32 v[72:73], v[72:73], v[122:123], v[132:133]
	v_pk_fma_f32 v[40:41], v[40:41], v[42:43], v[140:141]
	v_pk_fma_f32 v[68:69], v[104:105], v[106:107], v[68:69]
	v_pk_mul_f32 v[40:41], v[40:41], s[34:35] op_sel_hi:[1,0]
	v_pk_mul_f32 v[72:73], v[72:73], s[34:35] op_sel_hi:[1,0]
	v_pk_fma_f32 v[36:37], v[94:95], v[36:37], v[40:41]
	v_pk_add_f32 v[104:105], v[114:115], 1.0 op_sel_hi:[1,0]
	v_add_f32_e32 v40, 0, v36
	v_add_f32_e32 v40, v40, v37
	v_add_f32_e32 v40, v40, v38
	v_add_f32_e32 v40, v40, v39
	v_add_f32_e32 v40, v40, v44
	v_add_f32_e32 v40, v40, v45
	v_add_f32_e32 v40, v40, v46
	v_pk_fma_f32 v[72:73], v[102:103], v[104:105], v[72:73]
	v_add_f32_e32 v40, v40, v47
	v_add_f32_e32 v40, v40, v72
	v_add_f32_e32 v40, v40, v73
	v_add_f32_e32 v40, v40, v68
	v_add_f32_e32 v40, v40, v69
	v_add_f32_e32 v40, v40, v62
	v_add_f32_e32 v40, v40, v63
	v_add_f32_e32 v40, v40, v56
	v_add_f32_e32 v40, v40, v57
	ds_bpermute_b32 v41, v2, v40
	ds_read_b128 v[4:7], v185 offset:11264
	global_load_dword v184, v187, s[12:13]
	ds_read_b128 v[12:15], v185 offset:10240
	global_load_dword v184, v187, s[12:13]
	ds_read_b128 v[20:23], v185 offset:9216
	global_load_dword v184, v187, s[12:13]
	ds_read_b128 v[28:31], v185 offset:8192
	global_load_dword v184, v187, s[12:13]
	s_nop 0
	ds_read_b128 v[8:11], v185 offset:15360
	global_load_dword v184, v187, s[90:91]
	ds_read_b128 v[16:19], v185 offset:14336
	global_load_dword v184, v187, s[90:91]
	ds_read_b128 v[24:27], v185 offset:13312
	global_load_dword v184, v187, s[90:91]
	s_nop 0
	ds_read_b128 v[32:35], v185 offset:12288
	global_load_dword v184, v187, s[90:91]
	s_waitcnt lgkmcnt(0)
	v_add_f32_e32 v40, v40, v41
	ds_bpermute_b32 v41, v1, v40
	s_waitcnt lgkmcnt(0)
	v_add_f32_e32 v40, v40, v41
	ds_bpermute_b32 v41, v74, v40
	s_waitcnt lgkmcnt(0)
	v_add_f32_e32 v40, v40, v41
	ds_bpermute_b32 v41, v75, v40
	s_waitcnt lgkmcnt(0)
	v_add_f32_e32 v40, v40, v41
	ds_bpermute_b32 v41, v126, v40
	s_waitcnt lgkmcnt(0)
	v_add_f32_e32 v40, v40, v41
	ds_bpermute_b32 v41, v127, v40
	s_waitcnt lgkmcnt(0)
	v_add_f32_e32 v40, v40, v41
	v_mul_f32_e32 v40, 0x3a800000, v40
	v_pk_add_f32 v[36:37], v[36:37], v[40:41] op_sel_hi:[1,0] neg_lo:[0,1] neg_hi:[0,1]
	v_pk_add_f32 v[38:39], v[38:39], v[40:41] op_sel_hi:[1,0] neg_lo:[0,1] neg_hi:[0,1]
	v_pk_mul_f32 v[42:43], v[36:37], v[36:37]
	v_pk_mul_f32 v[48:49], v[38:39], v[38:39]
	v_add_f32_e32 v42, v42, v43
	v_pk_add_f32 v[44:45], v[44:45], v[40:41] op_sel_hi:[1,0] neg_lo:[0,1] neg_hi:[0,1]
	v_add_f32_e32 v42, v48, v42
	v_pk_mul_f32 v[50:51], v[44:45], v[44:45]
	v_add_f32_e32 v42, v49, v42
	v_pk_add_f32 v[46:47], v[46:47], v[40:41] op_sel_hi:[1,0] neg_lo:[0,1] neg_hi:[0,1]
	v_add_f32_e32 v42, v50, v42
	v_pk_mul_f32 v[58:59], v[46:47], v[46:47]
	v_add_f32_e32 v42, v51, v42
	v_pk_add_f32 v[60:61], v[72:73], v[40:41] op_sel_hi:[1,0] neg_lo:[0,1] neg_hi:[0,1]
	v_add_f32_e32 v42, v58, v42
	v_pk_mul_f32 v[64:65], v[60:61], v[60:61]
	v_add_f32_e32 v42, v59, v42
	v_pk_add_f32 v[66:67], v[68:69], v[40:41] op_sel_hi:[1,0] neg_lo:[0,1] neg_hi:[0,1]
	v_add_f32_e32 v42, v64, v42
	v_pk_mul_f32 v[68:69], v[66:67], v[66:67]
	v_add_f32_e32 v42, v65, v42
	v_pk_add_f32 v[62:63], v[62:63], v[40:41] op_sel_hi:[1,0] neg_lo:[0,1] neg_hi:[0,1]
	v_add_f32_e32 v42, v68, v42
	v_pk_mul_f32 v[70:71], v[62:63], v[62:63]
	v_add_f32_e32 v42, v69, v42
	v_pk_add_f32 v[40:41], v[56:57], v[40:41] op_sel_hi:[1,0] neg_lo:[0,1] neg_hi:[0,1]
	v_add_f32_e32 v42, v70, v42
	v_pk_mul_f32 v[56:57], v[40:41], v[40:41]
	v_add_f32_e32 v42, v71, v42
	v_add_f32_e32 v42, v56, v42
	v_add_f32_e32 v42, v57, v42
	ds_bpermute_b32 v43, v2, v42
	s_waitcnt lgkmcnt(0)
	v_add_f32_e32 v42, v42, v43
	ds_bpermute_b32 v43, v1, v42
	s_waitcnt lgkmcnt(0)
	v_add_f32_e32 v42, v42, v43
	ds_bpermute_b32 v43, v74, v42
	s_waitcnt lgkmcnt(0)
	v_add_f32_e32 v42, v42, v43
	ds_bpermute_b32 v43, v75, v42
	s_waitcnt lgkmcnt(0)
	v_add_f32_e32 v42, v42, v43
	ds_bpermute_b32 v43, v126, v42
	s_waitcnt lgkmcnt(0)
	v_add_f32_e32 v42, v42, v43
	ds_bpermute_b32 v43, v127, v42
	s_waitcnt lgkmcnt(0)
	v_add_f32_e32 v42, v42, v43
	v_fmamk_f32 v42, v42, 0x3a800000, v204
	v_cmp_gt_f32_e32 vcc, s26, v42
	v_mul_f32_e32 v43, 0x4b800000, v42
	s_nop 0
	v_cndmask_b32_e32 v42, v42, v43, vcc
	v_rsq_f32_e32 v42, v42
	s_nop 0
	v_mul_f32_e32 v43, 0x45800000, v42
	v_cndmask_b32_e32 v42, v42, v43, vcc
	v_pk_mul_f32 v[36:37], v[36:37], v[42:43] op_sel_hi:[1,0]
	s_and_b64 vcc, exec, s[6:7]
	s_waitcnt lgkmcnt(0)
	s_waitcnt vmcnt(0)
	v_pk_fma_f32 v[28:29], v[28:29], v[36:37], v[32:33]
	v_pk_mul_f32 v[32:33], v[38:39], v[42:43] op_sel_hi:[1,0]
	s_nop 0
	v_pk_fma_f32 v[30:31], v[30:31], v[32:33], v[34:35]
	v_pk_mul_f32 v[32:33], v[44:45], v[42:43] op_sel_hi:[1,0]
	s_nop 0
	v_pk_fma_f32 v[20:21], v[20:21], v[32:33], v[24:25]
	v_pk_mul_f32 v[24:25], v[46:47], v[42:43] op_sel_hi:[1,0]
	s_nop 0
	v_pk_fma_f32 v[22:23], v[22:23], v[24:25], v[26:27]
	v_pk_mul_f32 v[24:25], v[60:61], v[42:43] op_sel_hi:[1,0]
	s_nop 0
	v_pk_fma_f32 v[12:13], v[12:13], v[24:25], v[16:17]
	v_pk_mul_f32 v[16:17], v[66:67], v[42:43] op_sel_hi:[1,0]
	s_nop 0
	v_pk_fma_f32 v[14:15], v[14:15], v[16:17], v[18:19]
	v_pk_mul_f32 v[16:17], v[62:63], v[42:43] op_sel_hi:[1,0]
	s_nop 0
	v_pk_fma_f32 v[4:5], v[4:5], v[16:17], v[8:9]
	v_pk_mul_f32 v[8:9], v[40:41], v[42:43] op_sel_hi:[1,0]
	s_nop 0
	v_pk_fma_f32 v[6:7], v[6:7], v[8:9], v[10:11]
	v_lshl_add_u64 v[8:9], s[20:21], 0, v[54:55]
	global_store_dwordx4 v[8:9], v[28:31], off
	global_store_dwordx4 v[8:9], v[20:23], off offset:16
	global_store_dwordx4 v[8:9], v[12:15], off offset:32
	global_store_dwordx4 v[8:9], v[4:7], off offset:48
	s_cbranch_vccnz .LBB0_981
	s_lshl_b64 s[0:1], s[0:1], 10
	s_mul_hi_i32 s3, s2, 0x6000
	s_mulk_i32 s2, 0x6000
	s_add_u32 s2, s70, s2
	s_addc_u32 s3, s71, s3
	v_lshl_add_u64 v[48:49], v[52:53], 2, s[2:3]
	s_mov_b64 s[2:3], 0x19000
	v_add_co_u32_e32 v32, vcc, s86, v48
	v_lshl_add_u64 v[24:25], v[48:49], 0, s[2:3]
	s_mov_b64 s[2:3], 0x18000
	v_addc_co_u32_e32 v33, vcc, 0, v49, vcc
	v_lshl_add_u64 v[44:45], v[48:49], 0, s[2:3]
	v_add_co_u32_e32 v48, vcc, s67, v48
	global_load_dwordx4 v[8:11], v[24:25], off offset:32
	global_load_dwordx4 v[16:19], v[24:25], off offset:16
	v_addc_co_u32_e32 v49, vcc, 0, v49, vcc
	global_load_dwordx4 v[24:27], v[24:25], off offset:48
	s_nop 0
	global_load_dwordx4 v[32:35], v[32:33], off
	s_nop 0
	ds_read_b128 v[36:39], v188 offset:5120
	global_load_dword v184, v187, s[70:71]
	ds_read_b128 v[40:43], v188 offset:7168
	global_load_dword v184, v187, s[70:71]
	s_nop 0
	ds_read_b128 v[44:47], v188 offset:6144
	global_load_dword v184, v187, s[70:71]
	s_lshl_b64 s[0:1], s[0:1], 1
	ds_read_b128 v[48:51], v188 offset:4096
	global_load_dword v184, v187, s[70:71]
	s_add_u32 s0, s76, s0
	s_addc_u32 s1, s77, s1
	v_lshl_add_u64 v[52:53], v[52:53], 1, s[0:1]
	s_waitcnt lgkmcnt(0)
	s_waitcnt vmcnt(7)
	v_pk_add_f32 v[8:9], v[8:9], 1.0 op_sel_hi:[1,0]
	s_waitcnt lgkmcnt(0)
	s_waitcnt vmcnt(6)
	v_pk_add_f32 v[16:17], v[16:17], 1.0 op_sel_hi:[1,0]
	v_pk_add_f32 v[18:19], v[18:19], 1.0 op_sel_hi:[1,0]
	v_pk_add_f32 v[10:11], v[10:11], 1.0 op_sel_hi:[1,0]
	s_waitcnt lgkmcnt(0)
	s_waitcnt vmcnt(5)
	v_pk_add_f32 v[24:25], v[24:25], 1.0 op_sel_hi:[1,0]
	s_waitcnt lgkmcnt(0)
	s_waitcnt vmcnt(4)
	v_pk_add_f32 v[32:33], v[32:33], 1.0 op_sel_hi:[1,0]
	v_pk_add_f32 v[34:35], v[34:35], 1.0 op_sel_hi:[1,0]
	v_pk_add_f32 v[26:27], v[26:27], 1.0 op_sel_hi:[1,0]
	s_waitcnt lgkmcnt(0)
	s_waitcnt vmcnt(3)
	v_pk_fma_f32 v[16:17], v[20:21], v[16:17], v[36:37]
	v_pk_fma_f32 v[18:19], v[22:23], v[18:19], v[38:39]
	s_waitcnt lgkmcnt(0)
	s_waitcnt vmcnt(1)
	v_pk_fma_f32 v[8:9], v[12:13], v[8:9], v[44:45]
	v_pk_fma_f32 v[10:11], v[14:15], v[10:11], v[46:47]
	v_pk_fma_f32 v[4:5], v[4:5], v[24:25], v[40:41]
	s_waitcnt lgkmcnt(0)
	s_waitcnt vmcnt(0)
	v_pk_fma_f32 v[14:15], v[28:29], v[32:33], v[48:49]
	v_pk_fma_f32 v[20:21], v[30:31], v[34:35], v[50:51]
	v_pk_fma_f32 v[12:13], v[6:7], v[26:27], v[42:43]
	v_cvt_pk_bf16_f32 v6, v16, v17
	v_cvt_pk_bf16_f32 v7, v18, v19
	v_cvt_pk_bf16_f32 v8, v8, v9
	v_cvt_pk_bf16_f32 v9, v10, v11
	v_cvt_pk_bf16_f32 v10, v4, v5
	v_cvt_pk_bf16_f32 v4, v14, v15
	v_cvt_pk_bf16_f32 v5, v20, v21
	v_cvt_pk_bf16_f32 v11, v12, v13
	global_store_dwordx4 v[52:53], v[4:7], off
	global_store_dwordx4 v[52:53], v[8:11], off offset:16
.LBB0_981:
	s_or_b32 s22, s96, 3
	s_add_i32 s0, s22, s35
	s_ashr_i32 s1, s0, 31
	s_lshr_b32 s1, s1, 19
	s_add_i32 s0, s0, s1
	s_ashr_i32 s2, s0, 13
	s_ashr_i32 s0, s2, 31
	s_add_u32 s1, s2, s87
	s_addc_u32 s0, s0, 0
	s_mulk_i32 s0, 0x6000
	s_mul_hi_u32 s3, s1, 0x6000
	v_mov_b32_e32 v4, v179
	s_add_i32 s3, s3, s0
	s_mulk_i32 s1, 0x6000
	s_add_u32 s0, s70, s1
	v_lshlrev_b32_e32 v20, 4, v4
	s_addc_u32 s1, s71, s3
	s_ashr_i32 s23, s22, 31
	v_readlane_b32 s36, v253, 60
	v_ashrrev_i32_e32 v21, 31, v20
	s_lshl_b64 s[26:27], s[22:23], 12
	v_readlane_b32 s38, v253, 62
	v_lshlrev_b64 v[4:5], 2, v[20:21]
	v_readlane_b32 s39, v253, 63
	s_add_u32 s20, s38, s26
	v_lshl_add_u64 v[22:23], s[0:1], 0, v[4:5]
	s_mov_b64 s[0:1], 0x5000
	s_addc_u32 s21, s39, s27
	v_lshl_add_u64 v[14:15], v[22:23], 0, s[0:1]
	s_lshl_b64 s[0:1], s[22:23], 3
	v_add_co_u32_e32 v22, vcc, s18, v22
	s_add_u32 s0, s64, s0
	s_nop 0
	v_addc_co_u32_e32 v23, vcc, 0, v23, vcc
	v_lshl_add_u64 v[18:19], s[20:21], 0, v[4:5]
	s_addc_u32 s1, s65, s1
	ds_read_b128 v[6:9], v188 offset:3072
	global_load_dword v184, v187, s[70:71]
	ds_read_b128 v[10:13], v188 offset:2048
	global_load_dword v184, v187, s[70:71]
	s_nop 0
	ds_read_b128 v[14:17], v188 offset:1024
	global_load_dword v184, v187, s[70:71]
	s_nop 0
	ds_read_b128 v[22:25], v188 offset:0
	global_load_dword v184, v187, s[70:71]
	s_nop 0
	global_load_dwordx2 v[94:95], v3, s[0:1]
	global_load_dwordx4 v[26:29], v[18:19], off
	global_load_dwordx4 v[30:33], v[18:19], off offset:16
	global_load_dwordx4 v[34:37], v[18:19], off offset:32
	global_load_dwordx4 v[38:41], v[18:19], off offset:48
	v_lshl_add_u64 v[70:71], s[28:29], 0, v[4:5]
	v_lshl_add_u64 v[18:19], s[16:17], 0, v[4:5]
	ds_read_b128 v[42:45], v185 offset:7168
	global_load_dword v184, v187, s[28:29]
	ds_read_b128 v[46:49], v185 offset:3072
	global_load_dword v184, v187, s[16:17]
	ds_read_b128 v[50:53], v185 offset:2048
	global_load_dword v184, v187, s[16:17]
	ds_read_b128 v[54:57], v185 offset:6144
	global_load_dword v184, v187, s[28:29]
	ds_read_b128 v[58:61], v185 offset:5120
	global_load_dword v184, v187, s[28:29]
	ds_read_b128 v[62:65], v185 offset:1024
	global_load_dword v184, v187, s[16:17]
	ds_read_b128 v[66:69], v185 offset:0
	global_load_dword v184, v187, s[16:17]
	s_nop 0
	ds_read_b128 v[70:73], v185 offset:4096
	global_load_dword v184, v187, s[28:29]
	v_readlane_b32 s40, v254, 0
	v_readlane_b32 s41, v254, 1
	v_readlane_b32 s42, v254, 2
	v_readlane_b32 s43, v254, 3
	v_readlane_b32 s40, v255, 42
	v_readlane_b32 s42, v255, 44
	s_add_u32 s20, s30, s26
	s_addc_u32 s21, s31, s27
	v_readlane_b32 s43, v255, 45
	s_and_b64 vcc, exec, s[6:7]
	v_readlane_b32 s37, v253, 61
	v_readlane_b32 s44, v254, 4
	v_readlane_b32 s45, v254, 5
	v_readlane_b32 s46, v254, 6
	v_readlane_b32 s47, v254, 7
	v_readlane_b32 s48, v254, 8
	v_readlane_b32 s49, v254, 9
	v_readlane_b32 s50, v254, 10
	v_readlane_b32 s51, v254, 11
	v_readlane_b32 s41, v255, 43
	s_waitcnt lgkmcnt(0)
	s_waitcnt vmcnt(13)
	v_pk_add_f32 v[18:19], v[24:25], 1.0 op_sel_hi:[1,0]
	v_pk_add_f32 v[22:23], v[22:23], 1.0 op_sel_hi:[1,0]
	s_waitcnt lgkmcnt(0)
	s_waitcnt vmcnt(11)
	v_pk_add_f32 v[24:25], v[26:27], v[94:95] op_sel_hi:[1,0] neg_lo:[0,1] neg_hi:[0,1]
	v_pk_add_f32 v[26:27], v[28:29], v[94:95] op_sel_hi:[1,0] neg_lo:[0,1] neg_hi:[0,1]
	s_waitcnt lgkmcnt(0)
	s_waitcnt vmcnt(10)
	v_pk_add_f32 v[28:29], v[30:31], v[94:95] op_sel_hi:[1,0] neg_lo:[0,1] neg_hi:[0,1]
	v_pk_add_f32 v[30:31], v[32:33], v[94:95] op_sel_hi:[1,0] neg_lo:[0,1] neg_hi:[0,1]
	s_waitcnt lgkmcnt(0)
	s_waitcnt vmcnt(9)
	v_pk_add_f32 v[32:33], v[34:35], v[94:95] op_sel_hi:[1,0] neg_lo:[0,1] neg_hi:[0,1]
	v_pk_add_f32 v[34:35], v[36:37], v[94:95] op_sel_hi:[1,0] neg_lo:[0,1] neg_hi:[0,1]
	s_waitcnt lgkmcnt(0)
	s_waitcnt vmcnt(8)
	v_pk_add_f32 v[36:37], v[38:39], v[94:95] op_sel_hi:[1,0] neg_lo:[0,1] neg_hi:[0,1]
	v_pk_add_f32 v[38:39], v[40:41], v[94:95] op_sel_hi:[1,0] neg_lo:[0,1] neg_hi:[0,1]
	v_pk_mul_f32 v[24:25], v[94:95], v[24:25] op_sel:[1,0]
	v_pk_mul_f32 v[38:39], v[94:95], v[38:39] op_sel:[1,0]
	s_waitcnt lgkmcnt(0)
	s_waitcnt vmcnt(0)
	v_pk_fma_f32 v[24:25], v[66:67], v[24:25], v[70:71]
	v_pk_mul_f32 v[32:33], v[94:95], v[32:33] op_sel:[1,0]
	v_pk_mul_f32 v[26:27], v[94:95], v[26:27] op_sel:[1,0]
	v_pk_fma_f32 v[38:39], v[38:39], v[48:49], v[44:45]
	v_pk_mul_f32 v[24:25], v[24:25], s[34:35] op_sel_hi:[1,0]
	v_pk_add_f32 v[8:9], v[8:9], 1.0 op_sel_hi:[1,0]
	v_pk_mul_f32 v[36:37], v[94:95], v[36:37] op_sel:[1,0]
	v_pk_fma_f32 v[32:33], v[32:33], v[50:51], v[54:55]
	v_pk_fma_f32 v[26:27], v[26:27], v[68:69], v[72:73]
	v_pk_mul_f32 v[38:39], v[38:39], s[34:35] op_sel_hi:[1,0]
	v_pk_fma_f32 v[54:55], v[78:79], v[22:23], v[24:25]
	v_pk_mul_f32 v[34:35], v[94:95], v[34:35] op_sel:[1,0]
	v_pk_mul_f32 v[28:29], v[94:95], v[28:29] op_sel:[1,0]
	v_pk_fma_f32 v[36:37], v[36:37], v[46:47], v[42:43]
	v_pk_mul_f32 v[26:27], v[26:27], s[34:35] op_sel_hi:[1,0]
	v_pk_fma_f32 v[42:43], v[84:85], v[8:9], v[38:39]
	v_add_f32_e32 v8, 0, v54
	v_pk_fma_f32 v[34:35], v[34:35], v[52:53], v[56:57]
	v_pk_fma_f32 v[28:29], v[28:29], v[62:63], v[58:59]
	v_pk_fma_f32 v[52:53], v[80:81], v[18:19], v[26:27]
	v_add_f32_e32 v8, v8, v55
	v_pk_add_f32 v[14:15], v[14:15], 1.0 op_sel_hi:[1,0]
	v_pk_mul_f32 v[30:31], v[94:95], v[30:31] op_sel:[1,0]
	v_pk_mul_f32 v[28:29], v[28:29], s[34:35] op_sel_hi:[1,0]
	v_add_f32_e32 v8, v8, v52
	v_pk_fma_f32 v[30:31], v[30:31], v[64:65], v[60:61]
	v_pk_fma_f32 v[50:51], v[82:83], v[14:15], v[28:29]
	v_add_f32_e32 v8, v8, v53
	v_pk_add_f32 v[16:17], v[16:17], 1.0 op_sel_hi:[1,0]
	v_pk_mul_f32 v[30:31], v[30:31], s[34:35] op_sel_hi:[1,0]
	v_add_f32_e32 v8, v8, v50
	v_pk_fma_f32 v[48:49], v[86:87], v[16:17], v[30:31]
	v_add_f32_e32 v8, v8, v51
	v_pk_add_f32 v[10:11], v[10:11], 1.0 op_sel_hi:[1,0]
	v_pk_mul_f32 v[32:33], v[32:33], s[34:35] op_sel_hi:[1,0]
	v_add_f32_e32 v8, v8, v48
	v_pk_fma_f32 v[46:47], v[88:89], v[10:11], v[32:33]
	v_add_f32_e32 v8, v8, v49
	v_pk_add_f32 v[12:13], v[12:13], 1.0 op_sel_hi:[1,0]
	v_pk_mul_f32 v[34:35], v[34:35], s[34:35] op_sel_hi:[1,0]
	v_add_f32_e32 v8, v8, v46
	v_pk_fma_f32 v[44:45], v[90:91], v[12:13], v[34:35]
	v_add_f32_e32 v8, v8, v47
	v_pk_add_f32 v[6:7], v[6:7], 1.0 op_sel_hi:[1,0]
	v_pk_mul_f32 v[36:37], v[36:37], s[34:35] op_sel_hi:[1,0]
	v_add_f32_e32 v8, v8, v44
	v_pk_fma_f32 v[6:7], v[92:93], v[6:7], v[36:37]
	v_add_f32_e32 v8, v8, v45
	v_add_f32_e32 v8, v8, v6
	v_add_f32_e32 v8, v8, v7
	v_add_f32_e32 v8, v8, v42
	v_add_f32_e32 v8, v8, v43
	ds_bpermute_b32 v9, v2, v8
	v_lshl_add_u64 v[22:23], s[12:13], 0, v[4:5]
	v_lshl_add_u64 v[38:39], s[90:91], 0, v[4:5]
	s_waitcnt lgkmcnt(0)
	v_add_f32_e32 v8, v8, v9
	ds_bpermute_b32 v9, v1, v8
	s_waitcnt lgkmcnt(0)
	v_add_f32_e32 v8, v8, v9
	ds_bpermute_b32 v9, v74, v8
	s_waitcnt lgkmcnt(0)
	v_add_f32_e32 v8, v8, v9
	ds_bpermute_b32 v9, v75, v8
	s_waitcnt lgkmcnt(0)
	v_add_f32_e32 v26, v8, v9
	ds_bpermute_b32 v27, v126, v26
	ds_read_b128 v[8:11], v185 offset:11264
	global_load_dword v184, v187, s[12:13]
	ds_read_b128 v[12:15], v185 offset:10240
	global_load_dword v184, v187, s[12:13]
	ds_read_b128 v[16:19], v185 offset:9216
	global_load_dword v184, v187, s[12:13]
	s_nop 0
	ds_read_b128 v[22:25], v185 offset:8192
	global_load_dword v184, v187, s[12:13]
	s_waitcnt lgkmcnt(0)
	v_add_f32_e32 v56, v26, v27
	ds_read_b128 v[26:29], v185 offset:15360
	global_load_dword v184, v187, s[90:91]
	ds_read_b128 v[30:33], v185 offset:14336
	global_load_dword v184, v187, s[90:91]
	ds_read_b128 v[34:37], v185 offset:13312
	global_load_dword v184, v187, s[90:91]
	s_nop 0
	ds_read_b128 v[38:41], v185 offset:12288
	global_load_dword v184, v187, s[90:91]
	ds_bpermute_b32 v57, v127, v56
	s_waitcnt lgkmcnt(0)
	v_add_f32_e32 v56, v56, v57
	v_mul_f32_e32 v56, 0x3a800000, v56
	v_pk_add_f32 v[54:55], v[54:55], v[56:57] op_sel_hi:[1,0] neg_lo:[0,1] neg_hi:[0,1]
	v_pk_add_f32 v[52:53], v[52:53], v[56:57] op_sel_hi:[1,0] neg_lo:[0,1] neg_hi:[0,1]
	v_pk_add_f32 v[50:51], v[50:51], v[56:57] op_sel_hi:[1,0] neg_lo:[0,1] neg_hi:[0,1]
	v_pk_add_f32 v[48:49], v[48:49], v[56:57] op_sel_hi:[1,0] neg_lo:[0,1] neg_hi:[0,1]
	v_pk_add_f32 v[46:47], v[46:47], v[56:57] op_sel_hi:[1,0] neg_lo:[0,1] neg_hi:[0,1]
	v_pk_add_f32 v[44:45], v[44:45], v[56:57] op_sel_hi:[1,0] neg_lo:[0,1] neg_hi:[0,1]
	v_pk_add_f32 v[6:7], v[6:7], v[56:57] op_sel_hi:[1,0] neg_lo:[0,1] neg_hi:[0,1]
	v_pk_add_f32 v[42:43], v[42:43], v[56:57] op_sel_hi:[1,0] neg_lo:[0,1] neg_hi:[0,1]
	v_pk_mul_f32 v[56:57], v[54:55], v[54:55]
	v_pk_mul_f32 v[58:59], v[52:53], v[52:53]
	v_add_f32_e32 v56, v56, v57
	v_add_f32_e32 v56, v58, v56
	v_pk_mul_f32 v[60:61], v[50:51], v[50:51]
	v_add_f32_e32 v56, v59, v56
	v_add_f32_e32 v56, v60, v56
	v_pk_mul_f32 v[62:63], v[48:49], v[48:49]
	v_add_f32_e32 v56, v61, v56
	v_add_f32_e32 v56, v62, v56
	v_pk_mul_f32 v[64:65], v[46:47], v[46:47]
	v_add_f32_e32 v56, v63, v56
	v_add_f32_e32 v56, v64, v56
	v_pk_mul_f32 v[66:67], v[44:45], v[44:45]
	v_add_f32_e32 v56, v65, v56
	v_add_f32_e32 v56, v66, v56
	v_pk_mul_f32 v[68:69], v[6:7], v[6:7]
	v_add_f32_e32 v56, v67, v56
	v_add_f32_e32 v56, v68, v56
	v_pk_mul_f32 v[70:71], v[42:43], v[42:43]
	v_add_f32_e32 v56, v69, v56
	v_add_f32_e32 v56, v70, v56
	v_add_f32_e32 v56, v71, v56
	ds_bpermute_b32 v2, v2, v56
	s_waitcnt lgkmcnt(0)
	v_add_f32_e32 v2, v56, v2
	ds_bpermute_b32 v1, v1, v2
	v_lshl_add_u64 v[56:57], s[20:21], 0, v[4:5]
	s_waitcnt lgkmcnt(0)
	v_add_f32_e32 v1, v2, v1
	ds_bpermute_b32 v2, v74, v1
	s_waitcnt lgkmcnt(0)
	v_add_f32_e32 v1, v1, v2
	ds_bpermute_b32 v2, v75, v1
	s_waitcnt lgkmcnt(0)
	v_add_f32_e32 v1, v1, v2
	ds_bpermute_b32 v2, v126, v1
	s_waitcnt lgkmcnt(0)
	v_add_f32_e32 v1, v1, v2
	ds_bpermute_b32 v2, v127, v1
	s_waitcnt lgkmcnt(0)
	v_add_f32_e32 v1, v1, v2
	v_fmamk_f32 v1, v1, 0x3a800000, v204
	v_mul_f32_e32 v2, 0x4b800000, v1
	v_cmp_gt_f32_e64 s[0:1], s42, v1
	s_nop 1
	v_cndmask_b32_e64 v1, v1, v2, s[0:1]
	v_rsq_f32_e32 v1, v1
	s_nop 0
	v_mul_f32_e32 v2, 0x45800000, v1
	v_cndmask_b32_e64 v2, v1, v2, s[0:1]
	v_pk_mul_f32 v[4:5], v[54:55], v[2:3] op_sel_hi:[1,0]
	v_pk_mul_f32 v[52:53], v[52:53], v[2:3] op_sel_hi:[1,0]
	v_pk_mul_f32 v[50:51], v[50:51], v[2:3] op_sel_hi:[1,0]
	v_pk_mul_f32 v[48:49], v[48:49], v[2:3] op_sel_hi:[1,0]
	v_pk_mul_f32 v[46:47], v[46:47], v[2:3] op_sel_hi:[1,0]
	v_pk_mul_f32 v[44:45], v[44:45], v[2:3] op_sel_hi:[1,0]
	v_pk_mul_f32 v[54:55], v[6:7], v[2:3] op_sel_hi:[1,0]
	v_pk_mul_f32 v[42:43], v[42:43], v[2:3] op_sel_hi:[1,0]
	s_waitcnt lgkmcnt(0)
	s_waitcnt vmcnt(0)
	v_pk_fma_f32 v[4:5], v[22:23], v[4:5], v[38:39]
	v_pk_fma_f32 v[6:7], v[24:25], v[52:53], v[40:41]
	v_pk_fma_f32 v[16:17], v[16:17], v[50:51], v[34:35]
	v_pk_fma_f32 v[18:19], v[18:19], v[48:49], v[36:37]
	v_pk_fma_f32 v[12:13], v[12:13], v[46:47], v[30:31]
	v_pk_fma_f32 v[14:15], v[14:15], v[44:45], v[32:33]
	v_pk_fma_f32 v[8:9], v[8:9], v[54:55], v[26:27]
	v_pk_fma_f32 v[10:11], v[10:11], v[42:43], v[28:29]
	global_store_dwordx4 v[56:57], v[4:7], off
	global_store_dwordx4 v[56:57], v[16:19], off offset:16
	global_store_dwordx4 v[56:57], v[12:15], off offset:32
	global_store_dwordx4 v[56:57], v[8:11], off offset:48
	s_cbranch_vccnz .LBB0_937
	s_lshl_b64 s[0:1], s[22:23], 10
	s_mul_hi_i32 s3, s2, 0x6000
	s_mulk_i32 s2, 0x6000
	s_add_u32 s2, s70, s2
	s_addc_u32 s3, s71, s3
	v_lshl_add_u64 v[50:51], v[20:21], 2, s[2:3]
	s_mov_b64 s[2:3], 0x19000
	v_add_co_u32_e32 v34, vcc, s86, v50
	v_lshl_add_u64 v[30:31], v[50:51], 0, s[2:3]
	s_mov_b64 s[2:3], 0x18000
	v_addc_co_u32_e32 v35, vcc, 0, v51, vcc
	v_lshl_add_u64 v[46:47], v[50:51], 0, s[2:3]
	v_add_co_u32_e32 v50, vcc, s67, v50
	global_load_dwordx4 v[22:25], v[30:31], off offset:32
	global_load_dwordx4 v[26:29], v[30:31], off offset:16
	v_addc_co_u32_e32 v51, vcc, 0, v51, vcc
	global_load_dwordx4 v[30:33], v[30:31], off offset:48
	s_nop 0
	global_load_dwordx4 v[34:37], v[34:35], off
	s_nop 0
	ds_read_b128 v[38:41], v188 offset:5120
	global_load_dword v184, v187, s[70:71]
	ds_read_b128 v[42:45], v188 offset:7168
	global_load_dword v184, v187, s[70:71]
	s_nop 0
	ds_read_b128 v[46:49], v188 offset:6144
	global_load_dword v184, v187, s[70:71]
	s_lshl_b64 s[0:1], s[0:1], 1
	ds_read_b128 v[50:53], v188 offset:4096
	global_load_dword v184, v187, s[70:71]
	s_add_u32 s0, s76, s0
	s_addc_u32 s1, s77, s1
	v_lshl_add_u64 v[20:21], v[20:21], 1, s[0:1]
	s_waitcnt lgkmcnt(0)
	s_waitcnt vmcnt(7)
	v_pk_add_f32 v[22:23], v[22:23], 1.0 op_sel_hi:[1,0]
	s_waitcnt lgkmcnt(0)
	s_waitcnt vmcnt(6)
	v_pk_add_f32 v[26:27], v[26:27], 1.0 op_sel_hi:[1,0]
	v_pk_add_f32 v[28:29], v[28:29], 1.0 op_sel_hi:[1,0]
	s_waitcnt lgkmcnt(0)
	s_waitcnt vmcnt(4)
	v_pk_add_f32 v[34:35], v[34:35], 1.0 op_sel_hi:[1,0]
	v_pk_add_f32 v[36:37], v[36:37], 1.0 op_sel_hi:[1,0]
	v_pk_add_f32 v[24:25], v[24:25], 1.0 op_sel_hi:[1,0]
	v_pk_add_f32 v[30:31], v[30:31], 1.0 op_sel_hi:[1,0]
	v_pk_add_f32 v[32:33], v[32:33], 1.0 op_sel_hi:[1,0]
	s_waitcnt lgkmcnt(0)
	s_waitcnt vmcnt(3)
	v_pk_fma_f32 v[16:17], v[16:17], v[26:27], v[38:39]
	v_pk_fma_f32 v[18:19], v[18:19], v[28:29], v[40:41]
	s_waitcnt lgkmcnt(0)
	s_waitcnt vmcnt(0)
	v_pk_fma_f32 v[4:5], v[4:5], v[34:35], v[50:51]
	v_pk_fma_f32 v[26:27], v[6:7], v[36:37], v[52:53]
	v_pk_fma_f32 v[12:13], v[12:13], v[22:23], v[46:47]
	v_pk_fma_f32 v[14:15], v[14:15], v[24:25], v[48:49]
	v_pk_fma_f32 v[22:23], v[8:9], v[30:31], v[42:43]
	v_pk_fma_f32 v[24:25], v[10:11], v[32:33], v[44:45]
	v_cvt_pk_bf16_f32 v6, v16, v17
	v_cvt_pk_bf16_f32 v7, v18, v19
	v_cvt_pk_bf16_f32 v4, v4, v5
	v_cvt_pk_bf16_f32 v5, v26, v27
	v_cvt_pk_bf16_f32 v8, v12, v13
	v_cvt_pk_bf16_f32 v9, v14, v15
	v_cvt_pk_bf16_f32 v10, v22, v23
	v_cvt_pk_bf16_f32 v11, v24, v25
	global_store_dwordx4 v[20:21], v[4:7], off
	global_store_dwordx4 v[20:21], v[8:11], off offset:16
	s_branch .LBB0_937
